# GEMM1 phases: fp8 expert-table conversion stores (u rows, v slices) issued write-through (sc0 sc1)
# baseline (speedup 1.0000x reference)
; #define GAS __attribute__((address_space(1)))
; __device__ __forceinline__ void row_to_fp8_2(int lane, const float* xrow0, const float* xrow1, unsigned (&ow0)[4], unsigned (&ow1)[4], float& isc0, float& isc1) {
;     const GAS f32x4* xr0 = (const GAS f32x4*)xrow0 + lane; const GAS f32x4* xr1 = (const GAS f32x4*)xrow1 + lane;
;     f32x4 v0[4], v1[4];
; #pragma unroll
;     for (int j = 0; j < 4; ++j) { v0[j] = __builtin_nontemporal_load(xr0 + 64 * j); v1[j] = __builtin_nontemporal_load(xr1 + 64 * j); }
;     float m0 = 0.f, m1 = 0.f;
; #pragma unroll
;     for (int j = 0; j < 4; ++j) { m0 = fmaxf(m0, fmaxf(fmaxf(fabsf(v0[j].x), fabsf(v0[j].y)), fmaxf(fabsf(v0[j].z), fabsf(v0[j].w)))); m1 = fmaxf(m1, fmaxf(fmaxf(fabsf(v1[j].x), fabsf(v1[j].y)), fmaxf(fabsf(v1[j].z), fabsf(v1[j].w)))); }
; #pragma unroll
;     for (int o = 1; o < 64; o <<= 1) { m0 = fmaxf(m0, __shfl_xor(m0, o)); m1 = fmaxf(m1, __shfl_xor(m1, o)); }
;     int b0 = (int)((__float_as_uint(m0) >> 23) & 255u); b0 = b0 < 16 ? 16 : (b0 > 240 ? 240 : b0);
;     int b1 = (int)((__float_as_uint(m1) >> 23) & 255u); b1 = b1 < 16 ? 16 : (b1 > 240 ? 240 : b1);
;     const float s0 = __uint_as_float((unsigned)(261 - b0) << 23), s1 = __uint_as_float((unsigned)(261 - b1) << 23);
;     isc0 = __uint_as_float((unsigned)(b0 - 7) << 23); isc1 = __uint_as_float((unsigned)(b1 - 7) << 23);
; #pragma unroll
;     for (int j = 0; j < 4; ++j) { int p = __builtin_amdgcn_cvt_pk_fp8_f32(v0[j].x * s0, v0[j].y * s0, 0, false); p = __builtin_amdgcn_cvt_pk_fp8_f32(v0[j].z * s0, v0[j].w * s0, p, true); ow0[j] = (unsigned)p;
; __device__ __forceinline__ void tables_part(LAS unsigned char* lds, int wave, int lane, const float* pu, const float* pv, unsigned char* ws, int gw, int ngw, int wg, int nwg, int r0, int r1, int i0, int i1) {
;     for (int m = r0 + gw; m < r1; m += 2 * ngw) {
;         const int m1 = (m + ngw < r1) ? m + ngw : m;
;         float isc0, isc1; unsigned ow0[4], ow1[4];
;         row_to_fp8_2(lane, pu + (size_t)m * D, pu + (size_t)m1 * D, ow0, ow1, isc0, isc1);
; #pragma unroll
;         for (int j = 0; j < 4; ++j) { *((GAS unsigned*)(ws + WS_UT + (size_t)m * D + j * 256) + lane) = ow0[j]; *((GAS unsigned*)(ws + WS_UT + (size_t)m1 * D + j * 256) + lane) = ow1[j]; }
;         if (lane == 0) { ((float*)(ws + WS_ESC))[m] = isc0; ((float*)(ws + WS_ESC))[m1] = isc1; } }
.LBB0_179:
	global_load_dwordx4 v[14:17], v[8:9], off offset:-2048 nt
	global_load_dwordx4 v[18:21], v[8:9], off offset:-1024 nt
	global_load_dwordx4 v[22:25], v[8:9], off nt
	global_load_dwordx4 v[26:29], v[8:9], off offset:1024 nt
	s_add_i32 s7, s6, 0x400
	s_cmpk_lt_i32 s6, 0x3c00
	s_cselect_b32 s18, s7, s6
	s_ashr_i32 s19, s18, 31
	s_lshl_b64 s[20:21], s[18:19], 12
	v_lshl_add_u64 v[46:47], v[2:3], 0, s[20:21]
	global_load_dwordx4 v[30:33], v[46:47], off nt
	global_load_dwordx4 v[34:37], v[46:47], off offset:1024 nt
	global_load_dwordx4 v[38:41], v[46:47], off offset:2048 nt
	global_load_dwordx4 v[42:45], v[46:47], off offset:3072 nt
	v_mov_b32_e32 v55, 0
	s_lshl_b64 s[20:21], s[18:19], 10
	s_waitcnt vmcnt(0)
	v_max_f32_e64 v13, |v17|, |v17|
	v_max_f32_e64 v46, |v16|, |v16|
	v_max_f32_e64 v47, |v21|, |v21|
	v_max_f32_e64 v48, |v20|, |v20|
	v_max_f32_e64 v49, |v25|, |v25|
	v_max_f32_e64 v50, |v24|, |v24|
	v_max_f32_e64 v51, |v29|, |v29|
	v_max_f32_e64 v52, |v28|, |v28|
	v_max_f32_e32 v13, v46, v13
	v_max_f32_e32 v46, v48, v47
	v_max_f32_e32 v47, v50, v49
	v_max_f32_e32 v48, v52, v51
	v_max3_f32 v13, |v14|, |v15|, v13
	v_max3_f32 v46, |v18|, |v19|, v46
	v_max3_f32 v47, |v22|, |v23|, v47
	v_max3_f32 v48, |v26|, |v27|, v48
	v_max3_f32 v13, v13, 0, v46
	v_max3_f32 v13, v13, v47, v48
	ds_bpermute_b32 v46, v173, v13
	v_max_f32_e64 v47, |v33|, |v33|
	v_max_f32_e64 v48, |v32|, |v32|
	v_max_f32_e64 v49, |v37|, |v37|
	v_max_f32_e64 v50, |v36|, |v36|
	v_max_f32_e64 v51, |v41|, |v41|
	v_max_f32_e64 v52, |v40|, |v40|
	v_max_f32_e64 v53, |v45|, |v45|
	v_max_f32_e64 v54, |v44|, |v44|
	v_max_f32_e32 v47, v48, v47
	v_max_f32_e32 v48, v50, v49
	v_max_f32_e32 v49, v52, v51
	v_max_f32_e32 v50, v54, v53
	v_max3_f32 v47, |v30|, |v31|, v47
	v_max3_f32 v48, |v34|, |v35|, v48
	v_max3_f32 v49, |v38|, |v39|, v49
	v_max3_f32 v50, |v42|, |v43|, v50
	v_max3_f32 v47, v47, 0, v48
	v_max3_f32 v47, v47, v49, v50
	s_waitcnt lgkmcnt(0)
	v_max_f32_e32 v46, v46, v46
	ds_bpermute_b32 v48, v173, v47
	v_max_f32_e32 v13, v13, v46
	ds_bpermute_b32 v46, v174, v13
	v_mov_b32_e32 v49, 0
	v_mov_b32_e32 v53, 0
	s_waitcnt lgkmcnt(1)
	v_max_f32_e32 v48, v48, v48
	v_max_f32_e32 v47, v47, v48
	s_waitcnt lgkmcnt(0)
	v_max_f32_e32 v46, v46, v46
	ds_bpermute_b32 v48, v174, v47
	v_max_f32_e32 v13, v13, v46
	ds_bpermute_b32 v46, v175, v13
	v_mov_b32_e32 v51, 0
	v_mov_b32_e32 v54, 0
	s_waitcnt lgkmcnt(1)
	v_max_f32_e32 v48, v48, v48
	v_max_f32_e32 v47, v47, v48
	s_waitcnt lgkmcnt(0)
	v_max_f32_e32 v46, v46, v46
	ds_bpermute_b32 v48, v175, v47
	v_max_f32_e32 v13, v13, v46
	ds_bpermute_b32 v46, v176, v13
	v_mov_b32_e32 v50, 0
	v_mov_b32_e32 v52, 0
	s_waitcnt lgkmcnt(1)
	v_max_f32_e32 v48, v48, v48
	v_max_f32_e32 v47, v47, v48
	s_waitcnt lgkmcnt(0)
	v_max_f32_e32 v46, v46, v46
	ds_bpermute_b32 v48, v176, v47
	v_max_f32_e32 v13, v13, v46
	ds_bpermute_b32 v46, v10, v13
	s_waitcnt lgkmcnt(1)
	v_max_f32_e32 v48, v48, v48
	v_max_f32_e32 v47, v47, v48
	s_waitcnt lgkmcnt(0)
	v_max_f32_e32 v46, v46, v46
	ds_bpermute_b32 v48, v10, v47
	v_max_f32_e32 v13, v13, v46
	ds_bpermute_b32 v46, v11, v13
	s_waitcnt lgkmcnt(1)
	v_max_f32_e32 v48, v48, v48
	v_max_f32_e32 v47, v47, v48
	s_waitcnt lgkmcnt(0)
	v_max_f32_e32 v46, v46, v46
	v_max_f32_e32 v13, v13, v46
	ds_bpermute_b32 v46, v11, v47
	v_bfe_u32 v13, v13, 23, 8
	v_med3_u32 v13, v13, 16, v1
	v_lshlrev_b32_e32 v13, 23, v13
	v_sub_u32_e32 v48, 0x82800000, v13
	s_waitcnt lgkmcnt(0)
	v_max_f32_e32 v46, v46, v46
	v_mul_f32_e32 v14, v14, v48
	v_mul_f32_e32 v15, v15, v48
	v_mul_f32_e32 v22, v22, v48
	v_mul_f32_e32 v23, v23, v48
	v_max_f32_e32 v46, v47, v46
	v_cvt_pk_fp8_f32 v49, v14, v15
	v_cvt_pk_fp8_f32 v53, v22, v23
	v_bfe_u32 v14, v46, 23, 8
	v_med3_u32 v14, v14, 16, v1
	v_lshlrev_b32_e32 v14, 23, v14
	v_mul_f32_e32 v18, v18, v48
	v_mul_f32_e32 v19, v19, v48
	v_mul_f32_e32 v24, v24, v48
	v_mul_f32_e32 v25, v25, v48
	v_sub_u32_e32 v15, 0x82800000, v14
	v_cvt_pk_fp8_f32 v51, v18, v19
	v_cvt_pk_fp8_f32 v53, v24, v25 op_sel:[0,0,1]
	v_mul_f32_e32 v24, v38, v15
	v_mul_f32_e32 v25, v39, v15
	v_cvt_pk_fp8_f32 v54, v24, v25
	v_mul_f32_e32 v16, v16, v48
	v_mul_f32_e32 v17, v17, v48
	v_mul_f32_e32 v20, v20, v48
	v_mul_f32_e32 v21, v21, v48
	v_mul_f32_e32 v26, v26, v48
	v_mul_f32_e32 v27, v27, v48
	v_cvt_pk_fp8_f32 v49, v16, v17 op_sel:[0,0,1]
	v_mul_f32_e32 v16, v30, v15
	v_mul_f32_e32 v17, v31, v15
	v_cvt_pk_fp8_f32 v55, v26, v27
	v_cvt_pk_fp8_f32 v51, v20, v21 op_sel:[0,0,1]
	v_mul_f32_e32 v20, v34, v15
	v_mul_f32_e32 v21, v35, v15
	v_mul_f32_e32 v26, v40, v15
	v_cvt_pk_fp8_f32 v50, v16, v17
	v_mul_f32_e32 v16, v41, v15
	v_cvt_pk_fp8_f32 v52, v20, v21
	v_cvt_pk_fp8_f32 v54, v26, v16 op_sel:[0,0,1]
	v_mul_f32_e32 v16, v42, v15
	v_mul_f32_e32 v17, v43, v15
	v_mov_b32_e32 v20, 0
	v_cvt_pk_fp8_f32 v20, v16, v17
	v_mul_f32_e32 v18, v32, v15
	v_mul_f32_e32 v19, v33, v15
	v_mul_f32_e32 v22, v36, v15
	v_mul_f32_e32 v23, v37, v15
	v_cvt_pk_fp8_f32 v50, v18, v19 op_sel:[0,0,1]
	v_mul_f32_e32 v16, v44, v15
	v_mul_f32_e32 v15, v45, v15
	v_cvt_pk_fp8_f32 v20, v16, v15 op_sel:[0,0,1]
	v_lshl_add_u64 v[16:17], s[10:11], 0, v[6:7]
	v_cvt_pk_fp8_f32 v52, v22, v23 op_sel:[0,0,1]
	v_add_co_u32_e32 v16, vcc, 0x15000000, v16
	v_mul_f32_e32 v28, v28, v48
	v_mul_f32_e32 v29, v29, v48
	v_addc_co_u32_e32 v17, vcc, 0, v17, vcc
	v_lshl_add_u64 v[18:19], v[4:5], 0, s[20:21]
	v_cvt_pk_fp8_f32 v55, v28, v29 op_sel:[0,0,1]
	global_store_dword v[16:17], v49, off sc0 sc1
	global_store_dword v[18:19], v50, off sc0 sc1
	global_store_dword v[16:17], v51, off offset:256 sc0 sc1
	global_store_dword v[18:19], v52, off offset:256 sc0 sc1
	global_store_dword v[16:17], v53, off offset:512 sc0 sc1
	global_store_dword v[18:19], v54, off offset:512 sc0 sc1
	global_store_dword v[16:17], v55, off offset:768 sc0 sc1
	global_store_dword v[18:19], v20, off offset:768 sc0 sc1
	s_and_saveexec_b64 s[20:21], s[4:5]
	s_cbranch_execz .LBB0_178
	s_lshl_b64 s[18:19], s[18:19], 3
	s_add_u32 s18, s9, s18
	s_addc_u32 s19, s22, s19
	s_add_u32 s26, s10, s23
	v_add_u32_e32 v13, 0xfc800000, v13
	s_addc_u32 s27, s11, s24
	v_add_u32_e32 v14, 0xfc800000, v14
	global_store_dword v12, v13, s[26:27]
	global_store_dword v12, v14, s[18:19]
	s_branch .LBB0_178

; #define GAS __attribute__((address_space(1)))
; #define LAS __attribute__((address_space(3)))
; __device__ __forceinline__ void p0_vslice_item(LAS unsigned char* lds, int wave, int tid, const float* vt_l, unsigned char* VS_l, float* vsc_l, int item) {
;     ...
; #pragma unroll 1
;     for (int p = tid; p < 4096; p += 512) { const int cs = p >> 5, k = p & 31;
;         const mk_u32x2 a = *(const LAS mk_u32x2*)(lds + (2 * k) * 1032 + cs * 8), b = *(const LAS mk_u32x2*)(lds + (2 * k + 1) * 1032 + cs * 8);
;         *(GAS v4u*)(VS_l + ((size_t)cs * 16384 + e0 + 2 * k) * 8) = (v4u){a.x, a.y, b.x, b.y}; }
.LBB0_190:
	v_ashrrev_i32_e32 v16, 5, v5
	v_and_b32_e32 v9, 62, v4
	v_add_u32_e32 v12, 0x200, v5
	v_mul_u32_u24_e32 v13, 0x408, v9
	v_lshlrev_b32_e32 v14, 3, v16
	v_cmp_lt_i32_e32 vcc, s27, v5
	v_mov_b32_e32 v5, v12
	v_add3_u32 v12, 0, v13, v14
	v_ashrrev_i32_e32 v17, 31, v16
	ds_read2_b64 v[12:15], v12 offset1:129
	v_lshlrev_b64 v[16:17], 14, v[16:17]
	v_or_b32_e32 v16, s9, v16
	v_or_b32_e32 v16, v16, v9
	v_add_u32_e32 v4, 0x400, v4
	s_or_b64 s[20:21], vcc, s[20:21]
	v_lshl_add_u64 v[16:17], v[16:17], 3, s[16:17]
	s_waitcnt lgkmcnt(0)
	global_store_dwordx4 v[16:17], v[12:15], off sc0 sc1
	s_andn2_b64 exec, exec, s[20:21]
	s_cbranch_execnz .LBB0_190
	s_branch .LBB0_183

; #define GAS __attribute__((address_space(1)))
; __device__ __forceinline__ void row_to_fp8_2(int lane, const float* xrow0, const float* xrow1, unsigned (&ow0)[4], unsigned (&ow1)[4], float& isc0, float& isc1) {
;     const GAS f32x4* xr0 = (const GAS f32x4*)xrow0 + lane; const GAS f32x4* xr1 = (const GAS f32x4*)xrow1 + lane;
;     f32x4 v0[4], v1[4];
; #pragma unroll
;     for (int j = 0; j < 4; ++j) { v0[j] = __builtin_nontemporal_load(xr0 + 64 * j); v1[j] = __builtin_nontemporal_load(xr1 + 64 * j); }
;     float m0 = 0.f, m1 = 0.f;
; #pragma unroll
;     for (int j = 0; j < 4; ++j) { m0 = fmaxf(m0, fmaxf(fmaxf(fabsf(v0[j].x), fabsf(v0[j].y)), fmaxf(fabsf(v0[j].z), fabsf(v0[j].w)))); m1 = fmaxf(m1, fmaxf(fmaxf(fabsf(v1[j].x), fabsf(v1[j].y)), fmaxf(fabsf(v1[j].z), fabsf(v1[j].w)))); }
; #pragma unroll
;     for (int o = 1; o < 64; o <<= 1) { m0 = fmaxf(m0, __shfl_xor(m0, o)); m1 = fmaxf(m1, __shfl_xor(m1, o)); }
;     int b0 = (int)((__float_as_uint(m0) >> 23) & 255u); b0 = b0 < 16 ? 16 : (b0 > 240 ? 240 : b0);
;     int b1 = (int)((__float_as_uint(m1) >> 23) & 255u); b1 = b1 < 16 ? 16 : (b1 > 240 ? 240 : b1);
;     const float s0 = __uint_as_float((unsigned)(261 - b0) << 23), s1 = __uint_as_float((unsigned)(261 - b1) << 23);
;     isc0 = __uint_as_float((unsigned)(b0 - 7) << 23); isc1 = __uint_as_float((unsigned)(b1 - 7) << 23);
; #pragma unroll
;     for (int j = 0; j < 4; ++j) { int p = __builtin_amdgcn_cvt_pk_fp8_f32(v0[j].x * s0, v0[j].y * s0, 0, false); p = __builtin_amdgcn_cvt_pk_fp8_f32(v0[j].z * s0, v0[j].w * s0, p, true); ow0[j] = (unsigned)p;
; __device__ __forceinline__ void tables_part(LAS unsigned char* lds, int wave, int lane, const float* pu, const float* pv, unsigned char* ws, int gw, int ngw, int wg, int nwg, int r0, int r1, int i0, int i1) {
;     for (int m = r0 + gw; m < r1; m += 2 * ngw) {
;         const int m1 = (m + ngw < r1) ? m + ngw : m;
;         float isc0, isc1; unsigned ow0[4], ow1[4];
;         row_to_fp8_2(lane, pu + (size_t)m * D, pu + (size_t)m1 * D, ow0, ow1, isc0, isc1);
; #pragma unroll
;         for (int j = 0; j < 4; ++j) { *((GAS unsigned*)(ws + WS_UT + (size_t)m * D + j * 256) + lane) = ow0[j]; *((GAS unsigned*)(ws + WS_UT + (size_t)m1 * D + j * 256) + lane) = ow1[j]; }
;         if (lane == 0) { ((float*)(ws + WS_ESC))[m] = isc0; ((float*)(ws + WS_ESC))[m1] = isc1; } }
.LBB0_1175:
	global_load_dwordx4 v[14:17], v[8:9], off offset:-2048 nt
	global_load_dwordx4 v[18:21], v[8:9], off offset:-1024 nt
	global_load_dwordx4 v[22:25], v[8:9], off nt
	global_load_dwordx4 v[26:29], v[8:9], off offset:1024 nt
	s_add_i32 s7, s6, 0x400
	s_cmpk_lt_i32 s6, 0x7c00
	s_cselect_b32 s16, s7, s6
	s_ashr_i32 s17, s16, 31
	s_lshl_b64 s[18:19], s[16:17], 12
	v_lshl_add_u64 v[46:47], v[2:3], 0, s[18:19]
	global_load_dwordx4 v[30:33], v[46:47], off nt
	global_load_dwordx4 v[34:37], v[46:47], off offset:1024 nt
	global_load_dwordx4 v[38:41], v[46:47], off offset:2048 nt
	global_load_dwordx4 v[42:45], v[46:47], off offset:3072 nt
	v_mov_b32_e32 v55, 0
	s_lshl_b64 s[18:19], s[16:17], 10
	s_waitcnt vmcnt(0)
	v_max_f32_e64 v13, |v17|, |v17|
	v_max_f32_e64 v46, |v16|, |v16|
	v_max_f32_e64 v47, |v21|, |v21|
	v_max_f32_e64 v48, |v20|, |v20|
	v_max_f32_e64 v49, |v25|, |v25|
	v_max_f32_e64 v50, |v24|, |v24|
	v_max_f32_e64 v51, |v29|, |v29|
	v_max_f32_e64 v52, |v28|, |v28|
	v_max_f32_e32 v13, v46, v13
	v_max_f32_e32 v46, v48, v47
	v_max_f32_e32 v47, v50, v49
	v_max_f32_e32 v48, v52, v51
	v_max3_f32 v13, |v14|, |v15|, v13
	v_max3_f32 v46, |v18|, |v19|, v46
	v_max3_f32 v47, |v22|, |v23|, v47
	v_max3_f32 v48, |v26|, |v27|, v48
	v_max3_f32 v13, v13, 0, v46
	v_max3_f32 v13, v13, v47, v48
	ds_bpermute_b32 v46, v173, v13
	v_max_f32_e64 v47, |v33|, |v33|
	v_max_f32_e64 v48, |v32|, |v32|
	v_max_f32_e64 v49, |v37|, |v37|
	v_max_f32_e64 v50, |v36|, |v36|
	v_max_f32_e64 v51, |v41|, |v41|
	v_max_f32_e64 v52, |v40|, |v40|
	v_max_f32_e64 v53, |v45|, |v45|
	v_max_f32_e64 v54, |v44|, |v44|
	v_max_f32_e32 v47, v48, v47
	v_max_f32_e32 v48, v50, v49
	v_max_f32_e32 v49, v52, v51
	v_max_f32_e32 v50, v54, v53
	v_max3_f32 v47, |v30|, |v31|, v47
	v_max3_f32 v48, |v34|, |v35|, v48
	v_max3_f32 v49, |v38|, |v39|, v49
	v_max3_f32 v50, |v42|, |v43|, v50
	v_max3_f32 v47, v47, 0, v48
	v_max3_f32 v47, v47, v49, v50
	s_waitcnt lgkmcnt(0)
	v_max_f32_e32 v46, v46, v46
	ds_bpermute_b32 v48, v173, v47
	v_max_f32_e32 v13, v13, v46
	ds_bpermute_b32 v46, v174, v13
	v_mov_b32_e32 v49, 0
	v_mov_b32_e32 v53, 0
	s_waitcnt lgkmcnt(1)
	v_max_f32_e32 v48, v48, v48
	v_max_f32_e32 v47, v47, v48
	s_waitcnt lgkmcnt(0)
	v_max_f32_e32 v46, v46, v46
	ds_bpermute_b32 v48, v174, v47
	v_max_f32_e32 v13, v13, v46
	ds_bpermute_b32 v46, v175, v13
	v_mov_b32_e32 v51, 0
	v_mov_b32_e32 v54, 0
	s_waitcnt lgkmcnt(1)
	v_max_f32_e32 v48, v48, v48
	v_max_f32_e32 v47, v47, v48
	s_waitcnt lgkmcnt(0)
	v_max_f32_e32 v46, v46, v46
	ds_bpermute_b32 v48, v175, v47
	v_max_f32_e32 v13, v13, v46
	ds_bpermute_b32 v46, v176, v13
	v_mov_b32_e32 v50, 0
	v_mov_b32_e32 v52, 0
	s_waitcnt lgkmcnt(1)
	v_max_f32_e32 v48, v48, v48
	v_max_f32_e32 v47, v47, v48
	s_waitcnt lgkmcnt(0)
	v_max_f32_e32 v46, v46, v46
	ds_bpermute_b32 v48, v176, v47
	v_max_f32_e32 v13, v13, v46
	ds_bpermute_b32 v46, v10, v13
	s_waitcnt lgkmcnt(1)
	v_max_f32_e32 v48, v48, v48
	v_max_f32_e32 v47, v47, v48
	s_waitcnt lgkmcnt(0)
	v_max_f32_e32 v46, v46, v46
	ds_bpermute_b32 v48, v10, v47
	v_max_f32_e32 v13, v13, v46
	ds_bpermute_b32 v46, v11, v13
	s_waitcnt lgkmcnt(1)
	v_max_f32_e32 v48, v48, v48
	v_max_f32_e32 v47, v47, v48
	s_waitcnt lgkmcnt(0)
	v_max_f32_e32 v46, v46, v46
	v_max_f32_e32 v13, v13, v46
	ds_bpermute_b32 v46, v11, v47
	v_bfe_u32 v13, v13, 23, 8
	v_med3_u32 v13, v13, 16, v1
	v_lshlrev_b32_e32 v13, 23, v13
	v_sub_u32_e32 v48, 0x82800000, v13
	s_waitcnt lgkmcnt(0)
	v_max_f32_e32 v46, v46, v46
	v_mul_f32_e32 v14, v14, v48
	v_mul_f32_e32 v15, v15, v48
	v_mul_f32_e32 v22, v22, v48
	v_mul_f32_e32 v23, v23, v48
	v_max_f32_e32 v46, v47, v46
	v_cvt_pk_fp8_f32 v49, v14, v15
	v_cvt_pk_fp8_f32 v53, v22, v23
	v_bfe_u32 v14, v46, 23, 8
	v_med3_u32 v14, v14, 16, v1
	v_lshlrev_b32_e32 v14, 23, v14
	v_mul_f32_e32 v18, v18, v48
	v_mul_f32_e32 v19, v19, v48
	v_mul_f32_e32 v24, v24, v48
	v_mul_f32_e32 v25, v25, v48
	v_sub_u32_e32 v15, 0x82800000, v14
	v_cvt_pk_fp8_f32 v51, v18, v19
	v_cvt_pk_fp8_f32 v53, v24, v25 op_sel:[0,0,1]
	v_mul_f32_e32 v24, v38, v15
	v_mul_f32_e32 v25, v39, v15
	v_cvt_pk_fp8_f32 v54, v24, v25
	v_mul_f32_e32 v16, v16, v48
	v_mul_f32_e32 v17, v17, v48
	v_mul_f32_e32 v20, v20, v48
	v_mul_f32_e32 v21, v21, v48
	v_mul_f32_e32 v26, v26, v48
	v_mul_f32_e32 v27, v27, v48
	v_cvt_pk_fp8_f32 v49, v16, v17 op_sel:[0,0,1]
	v_mul_f32_e32 v16, v30, v15
	v_mul_f32_e32 v17, v31, v15
	v_cvt_pk_fp8_f32 v55, v26, v27
	v_cvt_pk_fp8_f32 v51, v20, v21 op_sel:[0,0,1]
	v_mul_f32_e32 v20, v34, v15
	v_mul_f32_e32 v21, v35, v15
	v_mul_f32_e32 v26, v40, v15
	v_cvt_pk_fp8_f32 v50, v16, v17
	v_mul_f32_e32 v16, v41, v15
	v_cvt_pk_fp8_f32 v52, v20, v21
	v_cvt_pk_fp8_f32 v54, v26, v16 op_sel:[0,0,1]
	v_mul_f32_e32 v16, v42, v15
	v_mul_f32_e32 v17, v43, v15
	v_mov_b32_e32 v20, 0
	v_cvt_pk_fp8_f32 v20, v16, v17
	v_mul_f32_e32 v18, v32, v15
	v_mul_f32_e32 v19, v33, v15
	v_mul_f32_e32 v22, v36, v15
	v_mul_f32_e32 v23, v37, v15
	v_cvt_pk_fp8_f32 v50, v18, v19 op_sel:[0,0,1]
	v_mul_f32_e32 v16, v44, v15
	v_mul_f32_e32 v15, v45, v15
	v_cvt_pk_fp8_f32 v20, v16, v15 op_sel:[0,0,1]
	v_lshl_add_u64 v[16:17], s[10:11], 0, v[6:7]
	v_cvt_pk_fp8_f32 v52, v22, v23 op_sel:[0,0,1]
	v_add_co_u32_e32 v16, vcc, 0x15000000, v16
	v_mul_f32_e32 v28, v28, v48
	v_mul_f32_e32 v29, v29, v48
	v_addc_co_u32_e32 v17, vcc, 0, v17, vcc
	v_lshl_add_u64 v[18:19], v[4:5], 0, s[18:19]
	v_cvt_pk_fp8_f32 v55, v28, v29 op_sel:[0,0,1]
	global_store_dword v[16:17], v49, off sc0 sc1
	global_store_dword v[18:19], v50, off sc0 sc1
	global_store_dword v[16:17], v51, off offset:256 sc0 sc1
	global_store_dword v[18:19], v52, off offset:256 sc0 sc1
	global_store_dword v[16:17], v53, off offset:512 sc0 sc1
	global_store_dword v[18:19], v54, off offset:512 sc0 sc1
	global_store_dword v[16:17], v55, off offset:768 sc0 sc1
	global_store_dword v[18:19], v20, off offset:768 sc0 sc1
	s_and_saveexec_b64 s[18:19], s[4:5]
	s_cbranch_execz .LBB0_1174
	s_lshl_b64 s[16:17], s[16:17], 3
	s_add_u32 s16, s20, s16
	s_addc_u32 s17, s21, s17
	s_add_u32 s24, s10, s22
	v_add_u32_e32 v13, 0xfc800000, v13
	s_addc_u32 s25, s11, s23
	v_add_u32_e32 v14, 0xfc800000, v14
	global_store_dword v12, v13, s[24:25]
	global_store_dword v12, v14, s[16:17]
	s_branch .LBB0_1174

; #define GAS __attribute__((address_space(1)))
; #define LAS __attribute__((address_space(3)))
; __device__ __forceinline__ void p0_vslice_item(LAS unsigned char* lds, int wave, int tid, const float* vt_l, unsigned char* VS_l, float* vsc_l, int item) {
;     ...
; #pragma unroll 1
;     for (int p = tid; p < 4096; p += 512) { const int cs = p >> 5, k = p & 31;
;         const mk_u32x2 a = *(const LAS mk_u32x2*)(lds + (2 * k) * 1032 + cs * 8), b = *(const LAS mk_u32x2*)(lds + (2 * k + 1) * 1032 + cs * 8);
;         *(GAS v4u*)(VS_l + ((size_t)cs * 16384 + e0 + 2 * k) * 8) = (v4u){a.x, a.y, b.x, b.y}; }
.LBB0_1186:
	v_ashrrev_i32_e32 v16, 5, v5
	v_and_b32_e32 v9, 62, v4
	v_add_u32_e32 v12, 0x200, v5
	v_mul_u32_u24_e32 v13, 0x408, v9
	v_lshlrev_b32_e32 v14, 3, v16
	v_cmp_lt_i32_e32 vcc, s26, v5
	v_mov_b32_e32 v5, v12
	v_add3_u32 v12, 0, v13, v14
	v_ashrrev_i32_e32 v17, 31, v16
	ds_read2_b64 v[12:15], v12 offset1:129
	v_lshlrev_b64 v[16:17], 14, v[16:17]
	v_or_b32_e32 v16, s8, v16
	v_or_b32_e32 v16, v16, v9
	v_add_u32_e32 v4, 0x400, v4
	s_or_b64 s[18:19], vcc, s[18:19]
	v_lshl_add_u64 v[16:17], v[16:17], 3, s[16:17]
	s_waitcnt lgkmcnt(0)
	global_store_dwordx4 v[16:17], v[12:15], off sc0 sc1
	s_andn2_b64 exec, exec, s[18:19]
	s_cbranch_execnz .LBB0_1186
	s_branch .LBB0_1179
